# MoE1/MoE2 per-unit tile search: one wave-wide LDS read + compare/popcount instead of a 6-step serial binary search
# speedup vs baseline: 1.0100x; 1.0023x over previous
;     __device__ __forceinline__ bool next(int i, Unit& u) const { const int L = i * G + c; if (L >= 64) return false; u.pm = L >> 1; u.pn = 0; u.a0 = L & 1; u.a1 = 0; return true; }
;     __device__ __forceinline__ bool next(int i, Unit& u) const {
;         const int TT = tab[64]; int rt, pn;
;         if (G == 256) { const int x = c & 7, y = c >> 3, Q = (TT + 7) >> 3, rl = i * 8 + (y >> 2); pn = y & 3; if (rl >= Q) return false; rt = x * Q + rl; }
;         else { const int L = i * G + c; rt = L >> 2; pn = L & 3; }
;         if (rt >= TT) return false;
;         int lo = 0, hi = 64;
;         while (hi - lo > 1) { const int mid = (lo + hi) >> 1; if (tab[mid] <= rt) lo = mid; else hi = mid; }
;         u.pm = rt; u.pn = pn; u.a0 = lo; u.a1 = rt - tab[lo]; return true;
.LBB0_900:
	s_mov_b64 s[22:23], 0
	s_and_b64 vcc, exec, s[4:5]
	s_cbranch_vccz .LBB0_905
	s_cmp_ge_i32 s19, s25
	s_cbranch_scc1 .LBB0_905
	v_mbcnt_lo_u32_b32 v2, -1, 0
	v_mbcnt_hi_u32_b32 v2, -1, v2
	v_lshlrev_b32_e32 v2, 2, v2
	v_add_u32_e32 v2, 0x24000, v2
	ds_read_b32 v2, v2
	s_and_b32 s20, s21, 3
	s_mov_b64 s[22:23], -1
	s_mov_b32 s55, s19
	s_waitcnt lgkmcnt(0)
	v_cmp_ge_i32_e64 s[4:5], s19, v2
	s_nop 0
	s_bcnt1_i32_b64 s18, s[4:5]
	s_add_i32 s18, s18, -1
	s_nop 0
	v_readlane_b32 s4, v2, s18
	s_nop 0
	s_sub_i32 s4, s19, s4
	v_mov_b32_e32 v157, s4

;     __device__ __forceinline__ bool next(int i, Unit& u) const { const int L = i * G + c; if (L >= 64) return false; u.pm = L >> 1; u.pn = 0; u.a0 = L & 1; u.a1 = 0; return true; }
;     __device__ __forceinline__ bool next(int i, Unit& u) const {
;         const int TT = tab[64]; int rt, pn;
;         if (G == 256) { const int x = c & 7, y = c >> 3, Q = (TT + 7) >> 3, rl = i * 8 + (y >> 2); pn = y & 3; if (rl >= Q) return false; rt = x * Q + rl; }
;         else { const int L = i * G + c; rt = L >> 2; pn = L & 3; }
;         if (rt >= TT) return false;
;         int lo = 0, hi = 64;
;         while (hi - lo > 1) { const int mid = (lo + hi) >> 1; if (tab[mid] <= rt) lo = mid; else hi = mid; }
;         u.pm = rt; u.pn = pn; u.a0 = lo; u.a1 = rt - tab[lo]; return true;
.LBB0_1010:
	s_mov_b64 s[12:13], 0
	s_and_b64 vcc, exec, s[4:5]
	s_cbranch_vccz .LBB0_1015
	s_cmp_ge_i32 s7, s25
	s_cbranch_scc1 .LBB0_1015
	v_mbcnt_lo_u32_b32 v2, -1, 0
	v_mbcnt_hi_u32_b32 v2, -1, v2
	v_lshlrev_b32_e32 v2, 2, v2
	v_add_u32_e32 v2, 0x24000, v2
	ds_read_b32 v2, v2
	s_and_b32 s22, s23, 3
	s_mov_b64 s[12:13], -1
	s_mov_b32 s24, s7
	s_waitcnt lgkmcnt(0)
	v_cmp_ge_i32_e64 s[4:5], s7, v2
	s_nop 0
	s_bcnt1_i32_b64 s55, s[4:5]
	s_add_i32 s55, s55, -1
	s_nop 0
	v_readlane_b32 s4, v2, s55
	s_nop 0
	s_sub_i32 s4, s7, s4
	v_mov_b32_e32 v173, s4
